# v55 + P12 diff-attention rescale path: 32 v_sub_f32 per rescale packed into 16 v_pk_add_f32 with negated broadcast operand (bitwise identical)
# baseline (speedup 1.0000x reference)
; template <int MODE, int DQK, int DV>
; __device__ __forceinline__ void attn_pass(LAS unsigned char* lds, const Tens& T, size_t rowbase, int q0, f32x16 (&o)[DV / 32], float& l_out, const int wave, QPre* qp = nullptr) {
;     ...
;             if (!POSTHOC || redo) {
;                 float ta = fmaxf(fmaxf(p[0][0], p[0][1]), p[0][2]), tb = fmaxf(fmaxf(p[1][0], p[1][1]), p[1][2]);
; #pragma unroll
;                 for (int rg = 3; rg < 15; rg += 2) { ta = fmaxf(fmaxf(ta, p[0][rg]), p[0][rg + 1]); tb = fmaxf(fmaxf(tb, p[1][rg]), p[1][rg + 1]); }
;                 float tmax = fmaxf(fmaxf(ta, tb), fmaxf(p[0][15], p[1][15]));
;                 { auto rr = __builtin_amdgcn_permlane32_swap(__float_as_uint(tmax), __float_as_uint(tmax), false, false); tmax = fmaxf(__uint_as_float(rr[0]), __uint_as_float(rr[1])); }
;                 if (POSTHOC || __builtin_expect(__any(tmax > THR), 0)) {
;                     const float delta = fmaxf(tmax, 0.f);
;                     m += delta;
;                     const float alpha = __builtin_amdgcn_exp2f(-delta);
;                     l *= alpha;
; #pragma unroll
;                     for (int kb = 0; kb < 2; ++kb)
; #pragma unroll
;                         for (int rg = 0; rg < 16; ++rg) p[kb][rg] -= delta;
; #pragma unroll
;                     for (int i = 0; i < NDB; ++i)
; #pragma unroll
;                         for (int rg = 0; rg < 16; ++rg) o[i][rg] *= alpha;
;                     if (MODE == AM_DIFF || MODE == AM_MLA) {
; #pragma unroll
;                         for (int rg = 0; rg < 16; ++rg) negm[rg] = -m;
;                     }
.LBB0_2450:
	s_nop 4
	v_max3_f32 v2, v96, v97, v98
	s_nop 0
	v_max3_f32 v3, v112, v113, v114
	v_max3_f32 v2, v2, v99, v100
	v_max3_f32 v3, v3, v115, v116
	v_max3_f32 v2, v2, v101, v102
	v_max3_f32 v3, v3, v117, v118
	v_max3_f32 v2, v2, v103, v104
	v_max3_f32 v3, v3, v119, v120
	v_max3_f32 v2, v2, v105, v106
	v_max3_f32 v3, v3, v121, v122
	v_max3_f32 v2, v2, v107, v108
	v_max3_f32 v3, v3, v123, v124
	v_max_f32_e32 v4, v127, v127
	v_max_f32_e32 v5, v111, v111
	v_max3_f32 v2, v2, v109, v110
	v_max3_f32 v3, v3, v125, v126
	v_max_f32_e32 v4, v5, v4
	v_max3_f32 v2, v2, v3, v4
	v_mov_b32_e32 v3, v2
	s_nop 1
	v_permlane32_swap_b32_e32 v2, v3
	v_max3_f32 v3, v2, v3, 0
	v_exp_f32_e64 v2, -v3
	v_add_f32_e32 v166, v166, v3
	v_xor_b32_e32 v80, 0x80000000, v166
	v_mov_b32_e32 v81, v80
	v_mul_f32_e32 v165, v165, v2
	v_pk_mul_f32 v[30:31], v[30:31], v[2:3] op_sel_hi:[1,0]
	v_pk_mul_f32 v[28:29], v[28:29], v[2:3] op_sel_hi:[1,0]
	v_pk_mul_f32 v[26:27], v[26:27], v[2:3] op_sel_hi:[1,0]
	v_pk_mul_f32 v[24:25], v[24:25], v[2:3] op_sel_hi:[1,0]
	v_pk_mul_f32 v[22:23], v[22:23], v[2:3] op_sel_hi:[1,0]
	v_pk_mul_f32 v[20:21], v[20:21], v[2:3] op_sel_hi:[1,0]
	v_pk_mul_f32 v[18:19], v[18:19], v[2:3] op_sel_hi:[1,0]
	v_pk_mul_f32 v[16:17], v[16:17], v[2:3] op_sel_hi:[1,0]
	v_pk_mul_f32 v[78:79], v[78:79], v[2:3] op_sel_hi:[1,0]
	v_pk_mul_f32 v[76:77], v[76:77], v[2:3] op_sel_hi:[1,0]
	v_pk_mul_f32 v[74:75], v[74:75], v[2:3] op_sel_hi:[1,0]
	v_pk_mul_f32 v[72:73], v[72:73], v[2:3] op_sel_hi:[1,0]
	v_pk_mul_f32 v[70:71], v[70:71], v[2:3] op_sel_hi:[1,0]
	v_pk_mul_f32 v[68:69], v[68:69], v[2:3] op_sel_hi:[1,0]
	v_pk_mul_f32 v[66:67], v[66:67], v[2:3] op_sel_hi:[1,0]
	v_pk_mul_f32 v[64:65], v[64:65], v[2:3] op_sel_hi:[1,0]
	v_pk_mul_f32 v[62:63], v[62:63], v[2:3] op_sel_hi:[1,0]
	v_pk_mul_f32 v[60:61], v[60:61], v[2:3] op_sel_hi:[1,0]
	v_pk_mul_f32 v[58:59], v[58:59], v[2:3] op_sel_hi:[1,0]
	v_pk_mul_f32 v[56:57], v[56:57], v[2:3] op_sel_hi:[1,0]
	v_pk_mul_f32 v[54:55], v[54:55], v[2:3] op_sel_hi:[1,0]
	v_pk_mul_f32 v[52:53], v[52:53], v[2:3] op_sel_hi:[1,0]
	v_pk_mul_f32 v[50:51], v[50:51], v[2:3] op_sel_hi:[1,0]
	v_pk_mul_f32 v[48:49], v[48:49], v[2:3] op_sel_hi:[1,0]
	v_pk_mul_f32 v[46:47], v[46:47], v[2:3] op_sel_hi:[1,0]
	v_pk_mul_f32 v[44:45], v[44:45], v[2:3] op_sel_hi:[1,0]
	v_pk_mul_f32 v[42:43], v[42:43], v[2:3] op_sel_hi:[1,0]
	v_pk_mul_f32 v[40:41], v[40:41], v[2:3] op_sel_hi:[1,0]
	v_pk_mul_f32 v[38:39], v[38:39], v[2:3] op_sel_hi:[1,0]
	v_pk_mul_f32 v[36:37], v[36:37], v[2:3] op_sel_hi:[1,0]
	v_pk_mul_f32 v[34:35], v[34:35], v[2:3] op_sel_hi:[1,0]
	v_pk_mul_f32 v[32:33], v[32:33], v[2:3] op_sel_hi:[1,0]
	v_mov_b32_e32 v82, v80
	v_mov_b32_e32 v83, v80
	v_mov_b32_e32 v84, v80
	v_mov_b32_e32 v85, v80
	v_mov_b32_e32 v86, v80
	v_mov_b32_e32 v87, v80
	v_mov_b32_e32 v88, v80
	v_mov_b32_e32 v89, v80
	v_mov_b32_e32 v90, v80
	v_mov_b32_e32 v91, v80
	v_mov_b32_e32 v92, v80
	v_mov_b32_e32 v93, v80
	v_mov_b32_e32 v94, v80
	v_mov_b32_e32 v95, v80
	v_pk_add_f32 v[126:127], v[126:127], v[2:3] op_sel:[0,1] op_sel_hi:[1,1] neg_lo:[0,1] neg_hi:[0,1]
	v_pk_add_f32 v[124:125], v[124:125], v[2:3] op_sel:[0,1] op_sel_hi:[1,1] neg_lo:[0,1] neg_hi:[0,1]
	v_pk_add_f32 v[122:123], v[122:123], v[2:3] op_sel:[0,1] op_sel_hi:[1,1] neg_lo:[0,1] neg_hi:[0,1]
	v_pk_add_f32 v[120:121], v[120:121], v[2:3] op_sel:[0,1] op_sel_hi:[1,1] neg_lo:[0,1] neg_hi:[0,1]
	v_pk_add_f32 v[118:119], v[118:119], v[2:3] op_sel:[0,1] op_sel_hi:[1,1] neg_lo:[0,1] neg_hi:[0,1]
	v_pk_add_f32 v[116:117], v[116:117], v[2:3] op_sel:[0,1] op_sel_hi:[1,1] neg_lo:[0,1] neg_hi:[0,1]
	v_pk_add_f32 v[114:115], v[114:115], v[2:3] op_sel:[0,1] op_sel_hi:[1,1] neg_lo:[0,1] neg_hi:[0,1]
	v_pk_add_f32 v[112:113], v[112:113], v[2:3] op_sel:[0,1] op_sel_hi:[1,1] neg_lo:[0,1] neg_hi:[0,1]
	v_pk_add_f32 v[110:111], v[110:111], v[2:3] op_sel:[0,1] op_sel_hi:[1,1] neg_lo:[0,1] neg_hi:[0,1]
	v_pk_add_f32 v[108:109], v[108:109], v[2:3] op_sel:[0,1] op_sel_hi:[1,1] neg_lo:[0,1] neg_hi:[0,1]
	v_pk_add_f32 v[106:107], v[106:107], v[2:3] op_sel:[0,1] op_sel_hi:[1,1] neg_lo:[0,1] neg_hi:[0,1]
	v_pk_add_f32 v[104:105], v[104:105], v[2:3] op_sel:[0,1] op_sel_hi:[1,1] neg_lo:[0,1] neg_hi:[0,1]
	v_pk_add_f32 v[102:103], v[102:103], v[2:3] op_sel:[0,1] op_sel_hi:[1,1] neg_lo:[0,1] neg_hi:[0,1]
	v_pk_add_f32 v[100:101], v[100:101], v[2:3] op_sel:[0,1] op_sel_hi:[1,1] neg_lo:[0,1] neg_hi:[0,1]
	v_pk_add_f32 v[98:99], v[98:99], v[2:3] op_sel:[0,1] op_sel_hi:[1,1] neg_lo:[0,1] neg_hi:[0,1]
	v_pk_add_f32 v[96:97], v[96:97], v[2:3] op_sel:[0,1] op_sel_hi:[1,1] neg_lo:[0,1] neg_hi:[0,1]
